# baseline (speedup 1.0000x reference)
_Z9ssim_mainPKfS0_S0_Pf:
	v_readfirstlane_b32 s29, v0
	s_load_dwordx4 s[4:7], s[0:1], 0x0
	s_load_dwordx4 s[8:11], s[0:1], 0x10
	s_mov_b32 s51, 0x44800000
	s_mov_b32 s38, 0
	s_mov_b32 s39, -1
	s_lshr_b32 s12, s29, 6
	s_and_b32 s13, s2, 7
	s_lshl_b32 s13, s13, 5
	s_lshr_b32 s14, s2, 3
	s_add_u32 s13, s13, s14
	s_lshr_b32 s14, s13, 3
	s_and_b32 s15, s13, 7
	s_lshl_b32 s16, s14, 20
	s_lshl_b32 s17, s15, 17
	s_add_u32 s16, s16, s17
	s_lshl_b32 s17, s12, 8
	s_add_u32 s16, s16, s17
	s_lshl_b32 s27, s12, 2
	s_add_u32 s27, s27, 0x10000
	v_and_b32_e32 v8, 63, v0
	v_and_b32_e32 v169, 15, v0
	v_bfe_u32 v164, v0, 4, 2
	v_lshrrev_b32_e32 v167, 2, v169
	v_lshlrev_b32_e32 v167, 5, v167
	v_and_b32_e32 v168, 1, v169
	v_lshl_or_b32 v167, v168, 4, v167
	v_bfe_u32 v168, v169, 1, 1
	v_lshl_or_b32 v167, v168, 7, v167
	v_lshl_or_b32 v9, v164, 14, v167
	v_and_b32_e32 v168, 1, v164
	v_lshl_or_b32 v23, v168, 14, v167
	v_lshrrev_b32_e32 v168, 1, v164
	v_lshl_or_b32 v23, v168, 13, v23
	v_add_u32_e32 v237, 0x1000, v9
	v_add_u32_e32 v238, 0x2000, v9
	v_add_u32_e32 v239, 0x3000, v9
	v_add_u32_e32 v240, 0x10000, v9
	v_add_u32_e32 v241, 0x11000, v9
	v_add_u32_e32 v242, 0x12000, v9
	v_add_u32_e32 v243, 0x13000, v9
	s_waitcnt lgkmcnt(0)
	s_load_dwordx8 s[40:47], s[8:9], 0x0
	s_load_dwordx2 s[48:49], s[8:9], 0x20
	s_load_dword s50, s[8:9], 0x28
	s_add_u32 s18, s4, s16
	s_addc_u32 s19, s5, 0
	s_add_u32 s20, s6, s16
	s_addc_u32 s21, s7, 0
	global_load_dwordx4 v[36:39], v9, s[18:19] offset:0 sc1 nt
	global_load_dwordx4 v[40:43], v9, s[18:19] offset:2048 sc1 nt
	global_load_dwordx4 v[68:71], v9, s[20:21] offset:0 sc1 nt
	global_load_dwordx4 v[72:75], v9, s[20:21] offset:2048 sc1 nt
	global_load_dwordx4 v[44:47], v237, s[18:19] offset:0 sc1 nt
	global_load_dwordx4 v[48:51], v237, s[18:19] offset:2048 sc1 nt
	global_load_dwordx4 v[76:79], v237, s[20:21] offset:0 sc1 nt
	global_load_dwordx4 v[80:83], v237, s[20:21] offset:2048 sc1 nt
	global_load_dwordx4 v[52:55], v238, s[18:19] offset:0 sc1 nt
	global_load_dwordx4 v[56:59], v238, s[18:19] offset:2048 sc1 nt
	global_load_dwordx4 v[84:87], v238, s[20:21] offset:0 sc1 nt
	global_load_dwordx4 v[88:91], v238, s[20:21] offset:2048 sc1 nt
	global_load_dwordx4 v[60:63], v239, s[18:19] offset:0 sc1 nt
	global_load_dwordx4 v[64:67], v239, s[18:19] offset:2048 sc1 nt
	global_load_dwordx4 v[92:95], v239, s[20:21] offset:0 sc1 nt
	global_load_dwordx4 v[96:99], v239, s[20:21] offset:2048 sc1 nt
	v_mov_b32_e32 v6, s27
	v_mov_b32_e32 v168, 0
	ds_write_b32 v6, v168 offset:0
	ds_write_b32 v6, v168 offset:32
	ds_write_b32 v6, v168 offset:64
	ds_write_b32 v6, v168 offset:96
	v_lshlrev_b32_e32 v167, 3, v164
	v_xor_b32_e32 v168, 16, v167
	v_sub_u32_e32 v165, v167, v169
	v_sub_u32_e32 v166, v168, v169
	v_add_u32_e32 v172, 0, v165
	v_min_u32_e32 v172, 11, v172
	v_lshlrev_b32_e32 v172, 2, v172
	v_add_u32_e32 v173, 1, v165
	v_min_u32_e32 v173, 11, v173
	v_lshlrev_b32_e32 v173, 2, v173
	v_add_u32_e32 v174, 2, v165
	v_min_u32_e32 v174, 11, v174
	v_lshlrev_b32_e32 v174, 2, v174
	v_add_u32_e32 v175, 3, v165
	v_min_u32_e32 v175, 11, v175
	v_lshlrev_b32_e32 v175, 2, v175
	v_add_u32_e32 v176, 4, v165
	v_min_u32_e32 v176, 11, v176
	v_lshlrev_b32_e32 v176, 2, v176
	v_add_u32_e32 v177, 5, v165
	v_min_u32_e32 v177, 11, v177
	v_lshlrev_b32_e32 v177, 2, v177
	v_add_u32_e32 v178, 6, v165
	v_min_u32_e32 v178, 11, v178
	v_lshlrev_b32_e32 v178, 2, v178
	v_add_u32_e32 v179, 7, v165
	v_min_u32_e32 v179, 11, v179
	v_lshlrev_b32_e32 v179, 2, v179
	v_add_u32_e32 v180, 0, v166
	v_min_u32_e32 v180, 11, v180
	v_lshlrev_b32_e32 v180, 2, v180
	v_add_u32_e32 v181, 1, v166
	v_min_u32_e32 v181, 11, v181
	v_lshlrev_b32_e32 v181, 2, v181
	v_add_u32_e32 v182, 2, v166
	v_min_u32_e32 v182, 11, v182
	v_lshlrev_b32_e32 v182, 2, v182
	v_add_u32_e32 v183, 3, v166
	v_min_u32_e32 v183, 11, v183
	v_lshlrev_b32_e32 v183, 2, v183
	v_add_u32_e32 v184, 4, v166
	v_min_u32_e32 v184, 11, v184
	v_lshlrev_b32_e32 v184, 2, v184
	v_add_u32_e32 v185, 5, v166
	v_min_u32_e32 v185, 11, v185
	v_lshlrev_b32_e32 v185, 2, v185
	v_add_u32_e32 v186, 6, v166
	v_min_u32_e32 v186, 11, v186
	v_lshlrev_b32_e32 v186, 2, v186
	v_add_u32_e32 v187, 7, v166
	v_min_u32_e32 v187, 11, v187
	v_lshlrev_b32_e32 v187, 2, v187
	global_load_dwordx4 v[100:103], v240, s[18:19] offset:0 sc1 nt
	global_load_dwordx4 v[104:107], v240, s[18:19] offset:2048 sc1 nt
	global_load_dwordx4 v[132:135], v240, s[20:21] offset:0 sc1 nt
	global_load_dwordx4 v[136:139], v240, s[20:21] offset:2048 sc1 nt
	global_load_dwordx4 v[108:111], v241, s[18:19] offset:0 sc1 nt
	global_load_dwordx4 v[112:115], v241, s[18:19] offset:2048 sc1 nt
	global_load_dwordx4 v[140:143], v241, s[20:21] offset:0 sc1 nt
	global_load_dwordx4 v[144:147], v241, s[20:21] offset:2048 sc1 nt
	global_load_dwordx4 v[116:119], v242, s[18:19] offset:0 sc1 nt
	global_load_dwordx4 v[120:123], v242, s[18:19] offset:2048 sc1 nt
	global_load_dwordx4 v[148:151], v242, s[20:21] offset:0 sc1 nt
	global_load_dwordx4 v[152:155], v242, s[20:21] offset:2048 sc1 nt
	global_load_dwordx4 v[124:127], v243, s[18:19] offset:0 sc1 nt
	global_load_dwordx4 v[128:131], v243, s[18:19] offset:2048 sc1 nt
	global_load_dwordx4 v[156:159], v243, s[20:21] offset:0 sc1 nt
	global_load_dwordx4 v[160:163], v243, s[20:21] offset:2048 sc1 nt
	s_cmp_eq_u32 s15, 7
	s_cselect_b32 s22, 0, 0x20000
	s_add_u32 s84, s18, s22
	s_addc_u32 s85, s19, 0
	s_add_u32 s86, s18, s22
	s_addc_u32 s87, s19, 0
	s_add_u32 s86, s86, 0x1000
	s_addc_u32 s87, s87, 0
	s_add_u32 s88, s20, s22
	s_addc_u32 s89, s21, 0
	s_add_u32 s90, s20, s22
	s_addc_u32 s91, s21, 0
	s_add_u32 s90, s90, 0x1000
	s_addc_u32 s91, s91, 0
	s_waitcnt lgkmcnt(0)
	v_writelane_b32 v171, s40, 0
	v_writelane_b32 v171, s41, 1
	v_writelane_b32 v171, s42, 2
	v_writelane_b32 v171, s43, 3
	v_writelane_b32 v171, s44, 4
	v_writelane_b32 v171, s45, 5
	v_writelane_b32 v171, s46, 6
	v_writelane_b32 v171, s47, 7
	v_writelane_b32 v171, s48, 8
	v_writelane_b32 v171, s49, 9
	v_writelane_b32 v171, s50, 10
	v_writelane_b32 v171, 0, 11
	v_fma_mixlo_f16 v171, v171, s51, 0
	ds_bpermute_b32 v188, v172, v171
	ds_bpermute_b32 v189, v173, v171
	ds_bpermute_b32 v190, v174, v171
	ds_bpermute_b32 v191, v175, v171
	ds_bpermute_b32 v192, v176, v171
	ds_bpermute_b32 v193, v177, v171
	ds_bpermute_b32 v194, v178, v171
	ds_bpermute_b32 v195, v179, v171
	v_mov_b32_e32 v229, 0x44800000
	v_fma_mixlo_f16 v228, s40, v229, 0
	v_cvt_f32_f16_e32 v228, v228
	v_cvt_f64_f32_e32 v[212:213], v228
	v_add_f64 v[212:213], v[212:213], 0
	v_fma_mixlo_f16 v228, s41, v229, 0
	v_cvt_f32_f16_e32 v228, v228
	v_cvt_f64_f32_e32 v[214:215], v228
	v_add_f64 v[212:213], v[212:213], v[214:215]
	v_fma_mixlo_f16 v228, s42, v229, 0
	v_cvt_f32_f16_e32 v228, v228
	v_cvt_f64_f32_e32 v[214:215], v228
	v_add_f64 v[212:213], v[212:213], v[214:215]
	v_fma_mixlo_f16 v228, s43, v229, 0
	v_cvt_f32_f16_e32 v228, v228
	v_cvt_f64_f32_e32 v[214:215], v228
	v_add_f64 v[212:213], v[212:213], v[214:215]
	v_fma_mixlo_f16 v228, s44, v229, 0
	v_cvt_f32_f16_e32 v228, v228
	v_cvt_f64_f32_e32 v[214:215], v228
	v_add_f64 v[212:213], v[212:213], v[214:215]
	v_fma_mixlo_f16 v228, s45, v229, 0
	v_cvt_f32_f16_e32 v228, v228
	v_cvt_f64_f32_e32 v[214:215], v228
	v_add_f64 v[212:213], v[212:213], v[214:215]
	v_fma_mixlo_f16 v228, s46, v229, 0
	v_cvt_f32_f16_e32 v228, v228
	v_cvt_f64_f32_e32 v[214:215], v228
	v_add_f64 v[212:213], v[212:213], v[214:215]
	v_fma_mixlo_f16 v228, s47, v229, 0
	v_cvt_f32_f16_e32 v228, v228
	v_cvt_f64_f32_e32 v[214:215], v228
	v_add_f64 v[212:213], v[212:213], v[214:215]
	v_fma_mixlo_f16 v228, s48, v229, 0
	v_cvt_f32_f16_e32 v228, v228
	v_cvt_f64_f32_e32 v[214:215], v228
	v_add_f64 v[212:213], v[212:213], v[214:215]
	v_fma_mixlo_f16 v228, s49, v229, 0
	v_cvt_f32_f16_e32 v228, v228
	v_cvt_f64_f32_e32 v[214:215], v228
	v_add_f64 v[212:213], v[212:213], v[214:215]
	v_fma_mixlo_f16 v228, s50, v229, 0
	v_cvt_f32_f16_e32 v228, v228
	v_cvt_f64_f32_e32 v[214:215], v228
	v_add_f64 v[212:213], v[212:213], v[214:215]
	s_waitcnt lgkmcnt(7)
	ds_bpermute_b32 v196, v180, v171
	ds_bpermute_b32 v197, v181, v171
	ds_bpermute_b32 v198, v182, v171
	ds_bpermute_b32 v199, v183, v171
	ds_bpermute_b32 v200, v184, v171
	ds_bpermute_b32 v201, v185, v171
	ds_bpermute_b32 v202, v186, v171
	ds_bpermute_b32 v203, v187, v171
	v_mul_f64 v[212:213], v[212:213], v[212:213]
	v_mul_f64 v[216:217], v[212:213], 0.5
	v_add_f64 v[218:219], v[216:217], v[216:217]
	s_mov_b32 s36, 0xeb1c432d
	s_mov_b32 s37, 0x3f1a36e2
	v_mul_f64 v[220:221], v[212:213], s[36:37]
	v_mul_f64 v[222:223], v[216:217], v[218:219]
	v_fmac_f64_e32 v[222:223], v[212:213], v[220:221]
	v_add_f64 v[224:225], v[212:213], v[212:213]
	s_mov_b32 s36, 0x487fcb92
	s_mov_b32 s37, 0x3f4d7dbf
	v_mul_f64 v[226:227], v[212:213], s[36:37]
	v_cvt_f32_f64_e32 v0, v[226:227]
	v_mov_b32_e32 v1, v0
	v_mov_b32_e32 v2, v0
	v_mov_b32_e32 v3, v0
	v_cvt_f32_f64_e32 v10, v[218:219]
	v_cvt_f32_f64_e32 v11, v[222:223]
	v_cvt_f32_f64_e32 v12, v[212:213]
	v_cvt_f32_f64_e32 v13, v[224:225]
	v_mul_f64 v[226:227], v[212:213], v[226:227]
	v_cvt_f32_f64_e32 v14, v[226:227]
	v_lshlrev_b32_e32 v167, 2, v164
	s_cmp_eq_u32 s12, 0
	s_cselect_b32 s23, 6, 64
	v_add_u32_e32 v168, 0, v167
	v_cmp_gt_u32_e32 vcc, s23, v168
	s_nop 1
	v_cndmask_b32_e64 v15, 0, 1.0, vcc
	v_add_u32_e32 v168, 1, v167
	v_cmp_gt_u32_e32 vcc, s23, v168
	s_nop 1
	v_cndmask_b32_e64 v16, 0, 1.0, vcc
	v_add_u32_e32 v168, 2, v167
	v_cmp_gt_u32_e32 vcc, s23, v168
	s_nop 1
	v_cndmask_b32_e64 v17, 0, 1.0, vcc
	v_add_u32_e32 v168, 3, v167
	v_cmp_gt_u32_e32 vcc, s23, v168
	s_nop 1
	v_cndmask_b32_e64 v18, 0, 1.0, vcc
	v_and_b32_e32 v167, 31, v8
	v_lshlrev_b32_e32 v167, 4, v167
	s_lshl_b32 s24, s12, 11
	s_add_i32 s25, s12, 7
	s_and_b32 s25, s25, 7
	s_lshl_b32 s26, s25, 11
	v_or_b32_e32 v4, s24, v167
	v_or_b32_e32 v5, s26, v167
	s_lshl_b32 s28, s25, 2
	s_add_u32 s28, s28, 0x10000
	v_mov_b32_e32 v7, s28
	v_mov_b32_e32 v19, 0
	v_mov_b32_e32 v20, 0
	v_mov_b32_e32 v21, 0
	v_mov_b32_e32 v22, 0
	s_waitcnt lgkmcnt(0)
	v_cmp_lt_u32_e64 s[32:33], 31, v8
	v_cmp_gt_u32_e64 s[34:35], 32, v8
	v_pack_b32_f16 v24, v188, v189
	v_pack_b32_f16 v25, v190, v191
	v_pack_b32_f16 v26, v192, v193
	v_pack_b32_f16 v27, v194, v195
	v_pack_b32_f16 v167, v196, v197
	v_cndmask_b32_e64 v28, 0, v167, s[32:33]
	v_cndmask_b32_e64 v32, 0, v167, s[34:35]
	v_pack_b32_f16 v167, v198, v199
	v_cndmask_b32_e64 v29, 0, v167, s[32:33]
	v_cndmask_b32_e64 v33, 0, v167, s[34:35]
	v_pack_b32_f16 v167, v200, v201
	v_cndmask_b32_e64 v30, 0, v167, s[32:33]
	v_cndmask_b32_e64 v34, 0, v167, s[34:35]
	v_pack_b32_f16 v167, v202, v203
	v_cndmask_b32_e64 v31, 0, v167, s[32:33]
	v_cndmask_b32_e64 v35, 0, v167, s[34:35]
	s_waitcnt lgkmcnt(0)
	s_waitcnt vmcnt(28)
	v_cvt_pk_f16_f32 v164, v36, v40
	v_cvt_pk_f16_f32 v180, v68, v72
	v_pk_add_f16 v164, v164, -0.5 op_sel_hi:[1,0]
	v_pk_add_f16 v180, v180, -0.5 op_sel_hi:[1,0]
	v_pk_mul_f16 v196, v180, v180
	v_pk_mul_f16 v212, v164, v180
	v_pk_fma_f16 v196, v164, v164, v196
	v_cvt_pk_f16_f32 v168, v37, v41
	v_cvt_pk_f16_f32 v184, v69, v73
	v_pk_add_f16 v168, v168, -0.5 op_sel_hi:[1,0]
	v_pk_add_f16 v184, v184, -0.5 op_sel_hi:[1,0]
	v_pk_mul_f16 v200, v184, v184
	v_pk_mul_f16 v216, v168, v184
	v_pk_fma_f16 v200, v168, v168, v200
	v_cvt_pk_f16_f32 v172, v38, v42
	v_cvt_pk_f16_f32 v188, v70, v74
	v_pk_add_f16 v172, v172, -0.5 op_sel_hi:[1,0]
	v_pk_add_f16 v188, v188, -0.5 op_sel_hi:[1,0]
	v_pk_mul_f16 v204, v188, v188
	v_pk_mul_f16 v220, v172, v188
	v_pk_fma_f16 v204, v172, v172, v204
	v_cvt_pk_f16_f32 v176, v39, v43
	v_cvt_pk_f16_f32 v192, v71, v75
	v_pk_add_f16 v176, v176, -0.5 op_sel_hi:[1,0]
	v_pk_add_f16 v192, v192, -0.5 op_sel_hi:[1,0]
	v_pk_mul_f16 v208, v192, v192
	v_pk_mul_f16 v224, v176, v192
	v_pk_fma_f16 v208, v176, v176, v208
	s_waitcnt vmcnt(24)
	v_cvt_pk_f16_f32 v165, v44, v48
	v_cvt_pk_f16_f32 v181, v76, v80
	v_pk_add_f16 v165, v165, -0.5 op_sel_hi:[1,0]
	v_pk_add_f16 v181, v181, -0.5 op_sel_hi:[1,0]
	v_pk_mul_f16 v197, v181, v181
	v_pk_mul_f16 v213, v165, v181
	v_pk_fma_f16 v197, v165, v165, v197
	v_cvt_pk_f16_f32 v169, v45, v49
	v_cvt_pk_f16_f32 v185, v77, v81
	v_pk_add_f16 v169, v169, -0.5 op_sel_hi:[1,0]
	v_pk_add_f16 v185, v185, -0.5 op_sel_hi:[1,0]
	v_pk_mul_f16 v201, v185, v185
	v_pk_mul_f16 v217, v169, v185
	v_pk_fma_f16 v201, v169, v169, v201
	v_cvt_pk_f16_f32 v173, v46, v50
	v_cvt_pk_f16_f32 v189, v78, v82
	v_pk_add_f16 v173, v173, -0.5 op_sel_hi:[1,0]
	v_pk_add_f16 v189, v189, -0.5 op_sel_hi:[1,0]
	v_pk_mul_f16 v205, v189, v189
	v_pk_mul_f16 v221, v173, v189
	v_pk_fma_f16 v205, v173, v173, v205
	v_cvt_pk_f16_f32 v177, v47, v51
	v_cvt_pk_f16_f32 v193, v79, v83
	v_pk_add_f16 v177, v177, -0.5 op_sel_hi:[1,0]
	v_pk_add_f16 v193, v193, -0.5 op_sel_hi:[1,0]
	v_pk_mul_f16 v209, v193, v193
	v_pk_mul_f16 v225, v177, v193
	v_pk_fma_f16 v209, v177, v177, v209
	s_waitcnt vmcnt(20)
	v_cvt_pk_f16_f32 v166, v52, v56
	v_cvt_pk_f16_f32 v182, v84, v88
	v_pk_add_f16 v166, v166, -0.5 op_sel_hi:[1,0]
	v_pk_add_f16 v182, v182, -0.5 op_sel_hi:[1,0]
	v_pk_mul_f16 v198, v182, v182
	v_pk_mul_f16 v214, v166, v182
	v_pk_fma_f16 v198, v166, v166, v198
	v_cvt_pk_f16_f32 v170, v53, v57
	v_cvt_pk_f16_f32 v186, v85, v89
	v_pk_add_f16 v170, v170, -0.5 op_sel_hi:[1,0]
	v_pk_add_f16 v186, v186, -0.5 op_sel_hi:[1,0]
	v_pk_mul_f16 v202, v186, v186
	v_pk_mul_f16 v218, v170, v186
	v_pk_fma_f16 v202, v170, v170, v202
	v_cvt_pk_f16_f32 v174, v54, v58
	v_cvt_pk_f16_f32 v190, v86, v90
	v_pk_add_f16 v174, v174, -0.5 op_sel_hi:[1,0]
	v_pk_add_f16 v190, v190, -0.5 op_sel_hi:[1,0]
	v_pk_mul_f16 v206, v190, v190
	v_pk_mul_f16 v222, v174, v190
	v_pk_fma_f16 v206, v174, v174, v206
	v_cvt_pk_f16_f32 v178, v55, v59
	v_cvt_pk_f16_f32 v194, v87, v91
	v_pk_add_f16 v178, v178, -0.5 op_sel_hi:[1,0]
	v_pk_add_f16 v194, v194, -0.5 op_sel_hi:[1,0]
	v_pk_mul_f16 v210, v194, v194
	v_pk_mul_f16 v226, v178, v194
	v_pk_fma_f16 v210, v178, v178, v210
	s_waitcnt vmcnt(16)
	v_cvt_pk_f16_f32 v167, v60, v64
	v_cvt_pk_f16_f32 v183, v92, v96
	v_pk_add_f16 v167, v167, -0.5 op_sel_hi:[1,0]
	v_pk_add_f16 v183, v183, -0.5 op_sel_hi:[1,0]
	v_pk_mul_f16 v199, v183, v183
	v_pk_mul_f16 v215, v167, v183
	v_pk_fma_f16 v199, v167, v167, v199
	v_cvt_pk_f16_f32 v171, v61, v65
	v_cvt_pk_f16_f32 v187, v93, v97
	v_pk_add_f16 v171, v171, -0.5 op_sel_hi:[1,0]
	v_pk_add_f16 v187, v187, -0.5 op_sel_hi:[1,0]
	v_pk_mul_f16 v203, v187, v187
	v_pk_mul_f16 v219, v171, v187
	v_pk_fma_f16 v203, v171, v171, v203
	v_cvt_pk_f16_f32 v175, v62, v66
	v_cvt_pk_f16_f32 v191, v94, v98
	v_pk_add_f16 v175, v175, -0.5 op_sel_hi:[1,0]
	v_pk_add_f16 v191, v191, -0.5 op_sel_hi:[1,0]
	v_pk_mul_f16 v207, v191, v191
	v_pk_mul_f16 v223, v175, v191
	v_pk_fma_f16 v207, v175, v175, v207
	v_cvt_pk_f16_f32 v179, v63, v67
	v_cvt_pk_f16_f32 v195, v95, v99
	v_pk_add_f16 v179, v179, -0.5 op_sel_hi:[1,0]
	v_pk_add_f16 v195, v195, -0.5 op_sel_hi:[1,0]
	v_pk_mul_f16 v211, v195, v195
	v_pk_mul_f16 v227, v179, v195
	v_pk_fma_f16 v211, v179, v179, v211
	v_mfma_f32_16x16x32_f16 v[68:71], v[164:167], v[24:27], 0
	v_mfma_f32_16x16x32_f16 v[72:75], v[168:171], v[24:27], 0
	v_mfma_f32_16x16x32_f16 v[76:79], v[172:175], v[24:27], 0
	v_mfma_f32_16x16x32_f16 v[80:83], v[176:179], v[24:27], 0
	v_mfma_f32_16x16x32_f16 v[84:87], v[180:183], v[24:27], 0
	v_mfma_f32_16x16x32_f16 v[88:91], v[184:187], v[24:27], 0
	v_mfma_f32_16x16x32_f16 v[92:95], v[188:191], v[24:27], 0
	v_mfma_f32_16x16x32_f16 v[96:99], v[192:195], v[24:27], 0
	s_nop 1
	v_cvt_pk_f16_f32 v36, v68, v72
	s_nop 0
	v_cvt_pk_f16_f32 v37, v76, v80
	v_cvt_pk_f16_f32 v38, v69, v73
	v_cvt_pk_f16_f32 v39, v77, v81
	v_cvt_pk_f16_f32 v40, v70, v74
	v_cvt_pk_f16_f32 v41, v78, v82
	v_cvt_pk_f16_f32 v42, v71, v75
	v_cvt_pk_f16_f32 v43, v79, v83
	v_mfma_f32_16x16x32_f16 v[68:71], v[196:199], v[24:27], 0
	v_mfma_f32_16x16x32_f16 v[72:75], v[200:203], v[24:27], 0
	v_mfma_f32_16x16x32_f16 v[76:79], v[204:207], v[24:27], 0
	v_mfma_f32_16x16x32_f16 v[80:83], v[208:211], v[24:27], 0
	v_cvt_pk_f16_f32 v44, v84, v88
	v_cvt_pk_f16_f32 v45, v92, v96
	v_cvt_pk_f16_f32 v46, v85, v89
	v_cvt_pk_f16_f32 v47, v93, v97
	v_cvt_pk_f16_f32 v48, v86, v90
	v_cvt_pk_f16_f32 v49, v94, v98
	v_cvt_pk_f16_f32 v50, v87, v91
	v_cvt_pk_f16_f32 v51, v95, v99
	v_mfma_f32_16x16x32_f16 v[84:87], v[212:215], v[24:27], 0
	v_mfma_f32_16x16x32_f16 v[88:91], v[216:219], v[24:27], 0
	v_mfma_f32_16x16x32_f16 v[92:95], v[220:223], v[24:27], 0
	v_mfma_f32_16x16x32_f16 v[96:99], v[224:227], v[24:27], 0
	v_cvt_pk_f16_f32 v52, v68, v72
	v_cvt_pk_f16_f32 v53, v76, v80
	v_cvt_pk_f16_f32 v54, v69, v73
	v_cvt_pk_f16_f32 v55, v77, v81
	v_cvt_pk_f16_f32 v56, v70, v74
	v_cvt_pk_f16_f32 v57, v78, v82
	v_cvt_pk_f16_f32 v58, v71, v75
	v_cvt_pk_f16_f32 v59, v79, v83
	v_cvt_pk_f16_f32 v60, v84, v88
	v_cvt_pk_f16_f32 v61, v92, v96
	v_cvt_pk_f16_f32 v62, v85, v89
	v_cvt_pk_f16_f32 v63, v93, v97
	v_cvt_pk_f16_f32 v64, v86, v90
	v_cvt_pk_f16_f32 v65, v94, v98
	v_cvt_pk_f16_f32 v66, v87, v91
	v_cvt_pk_f16_f32 v67, v95, v99
	s_mov_b64 exec, s[38:39]
	ds_write_b128 v4, v[40:43] offset:0
	ds_write_b128 v4, v[48:51] offset:512
	ds_write_b128 v4, v[56:59] offset:1024
	ds_write_b128 v4, v[64:67] offset:1536
	s_mov_b64 exec, -1
	v_mfma_f32_16x16x32_f16 v[68:71], v[24:27], v[36:39], 0
	v_mfma_f32_16x16x32_f16 v[72:75], v[24:27], v[44:47], 0
	v_mfma_f32_16x16x32_f16 v[76:79], v[24:27], v[52:55], v[0:3]
	v_mfma_f32_16x16x32_f16 v[80:83], v[24:27], v[60:63], 0
	v_mfma_f32_16x16x32_f16 v[84:87], v[28:31], v[36:39], 0
	v_mfma_f32_16x16x32_f16 v[88:91], v[28:31], v[44:47], 0
	v_mfma_f32_16x16x32_f16 v[92:95], v[28:31], v[52:55], v[0:3]
	v_mfma_f32_16x16x32_f16 v[96:99], v[28:31], v[60:63], 0
	v_mfma_f32_16x16x32_f16 v[84:87], v[32:35], v[40:43], v[84:87]
	v_mfma_f32_16x16x32_f16 v[88:91], v[32:35], v[48:51], v[88:91]
	v_mfma_f32_16x16x32_f16 v[92:95], v[32:35], v[56:59], v[92:95]
	v_mfma_f32_16x16x32_f16 v[96:99], v[32:35], v[64:67], v[96:99]
	s_waitcnt lgkmcnt(0)
	ds_write_b32 v6, v6 offset:0
	ds_read_b32 v9, v7 offset:0
	v_mul_f32_e32 v244, v68, v72
	v_mul_f32_e32 v250, v69, v73
	v_mul_f32_e64 v245, -v72, v72
	v_mul_f32_e64 v251, -v73, v73
	v_add_f32_e32 v246, v68, v72
	v_add_f32_e32 v252, v69, v73
	v_fma_f32 v245, -v68, v68, v245
	v_fma_f32 v251, -v69, v69, v251
	v_fma_f32 v247, v10, v246, v11
	v_fma_f32 v253, v10, v252, v11
	v_fma_f32 v246, v13, v80, v14
	v_fma_f32 v252, v13, v81, v14
	v_fma_f32 v248, v12, v76, v245
	v_fma_f32 v254, v12, v77, v251
	v_fma_f32 v249, 2.0, v244, v247
	v_fma_f32 v255, 2.0, v250, v253
	v_sub_f32_e32 v247, v247, v245
	v_sub_f32_e32 v253, v253, v251
	v_fma_f32 v246, -2.0, v244, v246
	v_fma_f32 v252, -2.0, v250, v252
	v_mul_f32_e32 v247, v247, v248
	v_mul_f32_e32 v253, v253, v254
	v_rcp_f32_e32 v247, v247
	v_rcp_f32_e32 v253, v253
	v_mul_f32_e32 v249, v249, v246
	v_mul_f32_e32 v255, v255, v252
	v_fma_f32 v19, v249, v247, v19
	v_fma_f32 v19, v255, v253, v19
	v_mul_f32_e32 v244, v70, v74
	v_mul_f32_e32 v250, v71, v75
	v_mul_f32_e64 v245, -v74, v74
	v_mul_f32_e64 v251, -v75, v75
	v_add_f32_e32 v246, v70, v74
	v_add_f32_e32 v252, v71, v75
	v_fma_f32 v245, -v70, v70, v245
	v_fma_f32 v251, -v71, v71, v251
	v_fma_f32 v247, v10, v246, v11
	v_fma_f32 v253, v10, v252, v11
	v_fma_f32 v246, v13, v82, v14
	v_fma_f32 v252, v13, v83, v14
	v_fma_f32 v248, v12, v78, v245
	v_fma_f32 v254, v12, v79, v251
	v_fma_f32 v249, 2.0, v244, v247
	v_fma_f32 v255, 2.0, v250, v253
	v_sub_f32_e32 v247, v247, v245
	v_sub_f32_e32 v253, v253, v251
	v_fma_f32 v246, -2.0, v244, v246
	v_fma_f32 v252, -2.0, v250, v252
	v_mul_f32_e32 v247, v247, v248
	v_mul_f32_e32 v253, v253, v254
	v_rcp_f32_e32 v247, v247
	v_rcp_f32_e32 v253, v253
	v_mul_f32_e32 v249, v249, v246
	v_mul_f32_e32 v255, v255, v252
	v_fma_f32 v20, v249, v247, v20
	v_fma_f32 v20, v255, v253, v20
	v_mfma_f32_16x16x32_f16 v[68:71], v[24:27], v[40:43], 0
	v_mfma_f32_16x16x32_f16 v[72:75], v[24:27], v[48:51], 0
	v_mfma_f32_16x16x32_f16 v[76:79], v[24:27], v[56:59], v[0:3]
	v_mfma_f32_16x16x32_f16 v[80:83], v[24:27], v[64:67], 0
	s_barrier
	ds_read_b32 v9, v7 offset:0
	s_waitcnt lgkmcnt(0)
	v_cmp_ne_u32_e32 vcc, 0, v9
	s_cbranch_vccnz .Lq_go_0
